# MoBA softmax-rescale decision: branch on the s_or lane mask directly instead of hipcc's cndmask 0/1 + v_cmp_ne ballot (section 7.12), 4 sites
# baseline (speedup 1.0000x reference)
.LBB0_496:
	v_max_f32_e32 v139, v49, v49
	v_max_f32_e32 v160, v48, v48
	v_max_f32_e32 v139, v160, v139
	v_max3_f32 v160, v50, v51, v33
	v_max3_f32 v139, v139, v32, v34
	v_max3_f32 v139, v139, v35, v52
	v_max3_f32 v160, v160, v54, v55
	v_max3_f32 v139, v139, v53, v36
	v_max3_f32 v160, v160, v38, v39
	v_max3_f32 v139, v139, v37, v56
	v_max3_f32 v160, v160, v58, v59
	v_max3_f32 v139, v139, v57, v40
	v_max3_f32 v160, v160, v42, v43
	v_max3_f32 v139, v139, v41, v60
	v_max3_f32 v160, v160, v62, v63
	v_max3_f32 v139, v139, v61, v44
	v_max3_f32 v160, v160, v46, v47
	v_max3_f32 v139, v139, v45, v160
	v_mov_b32_e32 v160, v139
	s_nop 1
	v_permlane32_swap_b32_e32 v139, v160
	v_max_f32_e32 v160, v160, v160
	v_max_f32_e32 v139, v139, v139
	v_max_f32_e32 v139, v139, v160
	v_cmp_lg_f32_e64 s[0:1], s23, v139
	s_xor_b64 s[6:7], s[44:45], -1
	s_and_b64 s[6:7], s[0:1], s[6:7]
	v_cmp_lt_f32_e32 vcc, s24, v139
	s_or_b64 vcc, vcc, s[6:7]
	s_cbranch_vccz .LBB0_500
	v_cndmask_b32_e64 v160, 0, v139, s[6:7]
	v_max_f32_e32 v139, v139, v139
	v_max_f32_e32 v139, 0, v139
	v_cndmask_b32_e64 v160, v160, v139, s[44:45]
	v_exp_f32_e64 v139, -v160
	s_nop 0
	v_cndmask_b32_e64 v139, v139, 1.0, s[6:7]
	s_and_saveexec_b64 s[6:7], s[4:5]
	ds_write_b32 v167, v139 offset:49152
	s_or_b64 exec, exec, s[6:7]
	s_waitcnt lgkmcnt(0)
	ds_read_b128 v[202:205], v168 offset:49152
	ds_read_b128 v[206:209], v168 offset:49184
	ds_read_b128 v[210:213], v168 offset:49216
	ds_read_b128 v[214:217], v168 offset:49248
	v_mul_f32_e32 v196, v196, v139
	v_pk_add_f32 v[48:49], v[48:49], v[160:161] op_sel_hi:[1,0] neg_lo:[0,1] neg_hi:[0,1]
	v_pk_add_f32 v[32:33], v[32:33], v[160:161] op_sel_hi:[1,0] neg_lo:[0,1] neg_hi:[0,1]
	v_pk_add_f32 v[50:51], v[50:51], v[160:161] op_sel_hi:[1,0] neg_lo:[0,1] neg_hi:[0,1]
	v_pk_add_f32 v[34:35], v[34:35], v[160:161] op_sel_hi:[1,0] neg_lo:[0,1] neg_hi:[0,1]
	v_pk_add_f32 v[52:53], v[52:53], v[160:161] op_sel_hi:[1,0] neg_lo:[0,1] neg_hi:[0,1]
	v_pk_add_f32 v[36:37], v[36:37], v[160:161] op_sel_hi:[1,0] neg_lo:[0,1] neg_hi:[0,1]
	v_pk_add_f32 v[54:55], v[54:55], v[160:161] op_sel_hi:[1,0] neg_lo:[0,1] neg_hi:[0,1]
	v_pk_add_f32 v[38:39], v[38:39], v[160:161] op_sel_hi:[1,0] neg_lo:[0,1] neg_hi:[0,1]
	v_pk_add_f32 v[56:57], v[56:57], v[160:161] op_sel_hi:[1,0] neg_lo:[0,1] neg_hi:[0,1]
	v_pk_add_f32 v[40:41], v[40:41], v[160:161] op_sel_hi:[1,0] neg_lo:[0,1] neg_hi:[0,1]
	v_pk_add_f32 v[58:59], v[58:59], v[160:161] op_sel_hi:[1,0] neg_lo:[0,1] neg_hi:[0,1]
	v_pk_add_f32 v[42:43], v[42:43], v[160:161] op_sel_hi:[1,0] neg_lo:[0,1] neg_hi:[0,1]
	v_pk_add_f32 v[60:61], v[60:61], v[160:161] op_sel_hi:[1,0] neg_lo:[0,1] neg_hi:[0,1]
	v_pk_add_f32 v[44:45], v[44:45], v[160:161] op_sel_hi:[1,0] neg_lo:[0,1] neg_hi:[0,1]
	v_pk_add_f32 v[62:63], v[62:63], v[160:161] op_sel_hi:[1,0] neg_lo:[0,1] neg_hi:[0,1]
	v_pk_add_f32 v[46:47], v[46:47], v[160:161] op_sel_hi:[1,0] neg_lo:[0,1] neg_hi:[0,1]
	v_add_f32_e32 v197, v197, v160
	s_or_b64 s[44:45], s[44:45], s[0:1]
	s_waitcnt lgkmcnt(0)
	v_pk_mul_f32 v[14:15], v[14:15], v[216:217]
	v_pk_mul_f32 v[10:11], v[10:11], v[212:213]
	v_pk_mul_f32 v[6:7], v[6:7], v[208:209]
	v_pk_mul_f32 v[2:3], v[2:3], v[204:205]
	v_pk_mul_f32 v[12:13], v[12:13], v[214:215]
	v_pk_mul_f32 v[8:9], v[8:9], v[210:211]
	v_pk_mul_f32 v[4:5], v[4:5], v[206:207]
	v_pk_mul_f32 v[0:1], v[0:1], v[202:203]
	v_pk_mul_f32 v[30:31], v[30:31], v[216:217]
	v_pk_mul_f32 v[26:27], v[26:27], v[212:213]
	v_pk_mul_f32 v[22:23], v[22:23], v[208:209]
	v_pk_mul_f32 v[18:19], v[18:19], v[204:205]
	v_pk_mul_f32 v[28:29], v[28:29], v[214:215]
	v_pk_mul_f32 v[24:25], v[24:25], v[210:211]
	v_pk_mul_f32 v[20:21], v[20:21], v[206:207]
	v_pk_mul_f32 v[16:17], v[16:17], v[202:203]

.LBB0_508:
	v_max_f32_e32 v96, v49, v49
	v_max_f32_e32 v97, v48, v48
	v_max_f32_e32 v96, v97, v96
	v_max3_f32 v97, v50, v51, v33
	v_max3_f32 v96, v96, v32, v34
	v_max3_f32 v96, v96, v35, v52
	v_max3_f32 v97, v97, v54, v55
	v_max3_f32 v96, v96, v53, v36
	v_max3_f32 v97, v97, v38, v39
	v_max3_f32 v96, v96, v37, v56
	v_max3_f32 v97, v97, v58, v59
	v_max3_f32 v96, v96, v57, v40
	v_max3_f32 v97, v97, v42, v43
	v_max3_f32 v96, v96, v41, v60
	v_max3_f32 v97, v97, v62, v63
	v_max3_f32 v96, v96, v61, v44
	v_max3_f32 v97, v97, v46, v47
	v_max3_f32 v96, v96, v45, v97
	v_mov_b32_e32 v97, v96
	s_nop 1
	v_permlane32_swap_b32_e32 v96, v97
	v_max_f32_e32 v97, v97, v97
	v_max_f32_e32 v96, v96, v96
	v_max_f32_e32 v96, v96, v97
	v_cmp_lg_f32_e32 vcc, s23, v96
	s_xor_b64 s[0:1], s[44:45], -1
	s_and_b64 s[0:1], vcc, s[0:1]
	v_cmp_lt_f32_e32 vcc, s24, v96
	s_or_b64 vcc, vcc, s[0:1]
	s_cbranch_vccz .LBB0_512
	v_cndmask_b32_e64 v97, 0, v96, s[0:1]
	v_max_f32_e32 v96, v96, v96
	v_max_f32_e32 v96, 0, v96
	v_cndmask_b32_e64 v96, v97, v96, s[44:45]
	v_exp_f32_e64 v97, -v96
	s_nop 0
	v_cndmask_b32_e64 v97, v97, 1.0, s[0:1]
	s_and_saveexec_b64 s[0:1], s[4:5]
	ds_write_b32 v167, v97 offset:49152
	s_or_b64 exec, exec, s[0:1]
	s_waitcnt lgkmcnt(0)
	v_mul_f32_e32 v196, v196, v97
	v_pk_add_f32 v[48:49], v[48:49], v[96:97] op_sel_hi:[1,0] neg_lo:[0,1] neg_hi:[0,1]
	v_pk_add_f32 v[32:33], v[32:33], v[96:97] op_sel_hi:[1,0] neg_lo:[0,1] neg_hi:[0,1]
	v_pk_add_f32 v[50:51], v[50:51], v[96:97] op_sel_hi:[1,0] neg_lo:[0,1] neg_hi:[0,1]
	v_pk_add_f32 v[34:35], v[34:35], v[96:97] op_sel_hi:[1,0] neg_lo:[0,1] neg_hi:[0,1]
	v_pk_add_f32 v[52:53], v[52:53], v[96:97] op_sel_hi:[1,0] neg_lo:[0,1] neg_hi:[0,1]
	v_pk_add_f32 v[36:37], v[36:37], v[96:97] op_sel_hi:[1,0] neg_lo:[0,1] neg_hi:[0,1]
	v_pk_add_f32 v[54:55], v[54:55], v[96:97] op_sel_hi:[1,0] neg_lo:[0,1] neg_hi:[0,1]
	v_pk_add_f32 v[38:39], v[38:39], v[96:97] op_sel_hi:[1,0] neg_lo:[0,1] neg_hi:[0,1]
	v_pk_add_f32 v[56:57], v[56:57], v[96:97] op_sel_hi:[1,0] neg_lo:[0,1] neg_hi:[0,1]
	v_pk_add_f32 v[40:41], v[40:41], v[96:97] op_sel_hi:[1,0] neg_lo:[0,1] neg_hi:[0,1]
	v_pk_add_f32 v[58:59], v[58:59], v[96:97] op_sel_hi:[1,0] neg_lo:[0,1] neg_hi:[0,1]
	v_pk_add_f32 v[42:43], v[42:43], v[96:97] op_sel_hi:[1,0] neg_lo:[0,1] neg_hi:[0,1]
	v_pk_add_f32 v[60:61], v[60:61], v[96:97] op_sel_hi:[1,0] neg_lo:[0,1] neg_hi:[0,1]
	v_pk_add_f32 v[44:45], v[44:45], v[96:97] op_sel_hi:[1,0] neg_lo:[0,1] neg_hi:[0,1]
	v_pk_add_f32 v[62:63], v[62:63], v[96:97] op_sel_hi:[1,0] neg_lo:[0,1] neg_hi:[0,1]
	v_pk_add_f32 v[46:47], v[46:47], v[96:97] op_sel_hi:[1,0] neg_lo:[0,1] neg_hi:[0,1]
	ds_read_b128 v[96:99], v168 offset:49152
	ds_read_b128 v[100:103], v168 offset:49184
	ds_read_b128 v[104:107], v168 offset:49216
	ds_read_b128 v[108:111], v168 offset:49248
	s_waitcnt lgkmcnt(0)
	v_pk_mul_f32 v[2:3], v[2:3], v[98:99]
	v_pk_mul_f32 v[6:7], v[6:7], v[102:103]
	v_pk_mul_f32 v[10:11], v[10:11], v[106:107]
	v_pk_mul_f32 v[14:15], v[14:15], v[110:111]
	v_pk_mul_f32 v[12:13], v[12:13], v[108:109]
	v_pk_mul_f32 v[8:9], v[8:9], v[104:105]
	v_pk_mul_f32 v[4:5], v[4:5], v[100:101]
	v_pk_mul_f32 v[0:1], v[0:1], v[96:97]
	v_pk_mul_f32 v[30:31], v[30:31], v[110:111]
	v_pk_mul_f32 v[26:27], v[26:27], v[106:107]
	v_pk_mul_f32 v[22:23], v[22:23], v[102:103]
	v_pk_mul_f32 v[18:19], v[18:19], v[98:99]
	v_pk_mul_f32 v[28:29], v[28:29], v[108:109]
	v_pk_mul_f32 v[24:25], v[24:25], v[104:105]
	v_pk_mul_f32 v[20:21], v[20:21], v[100:101]
	v_pk_mul_f32 v[16:17], v[16:17], v[96:97]

.LBB0_3035:
	v_max_f32_e32 v139, v49, v49
	v_max_f32_e32 v160, v48, v48
	v_max_f32_e32 v139, v160, v139
	v_max3_f32 v160, v50, v51, v33
	v_max3_f32 v139, v139, v32, v34
	v_max3_f32 v139, v139, v35, v52
	v_max3_f32 v160, v160, v54, v55
	v_max3_f32 v139, v139, v53, v36
	v_max3_f32 v160, v160, v38, v39
	v_max3_f32 v139, v139, v37, v56
	v_max3_f32 v160, v160, v58, v59
	v_max3_f32 v139, v139, v57, v40
	v_max3_f32 v160, v160, v42, v43
	v_max3_f32 v139, v139, v41, v60
	v_max3_f32 v160, v160, v62, v63
	v_max3_f32 v139, v139, v61, v44
	v_max3_f32 v160, v160, v46, v47
	v_max3_f32 v139, v139, v45, v160
	v_mov_b32_e32 v160, v139
	s_nop 1
	v_permlane32_swap_b32_e32 v139, v160
	v_max_f32_e32 v160, v160, v160
	v_max_f32_e32 v139, v139, v139
	v_max_f32_e32 v139, v139, v160
	v_cmp_lg_f32_e64 s[6:7], s48, v139
	s_xor_b64 s[0:1], s[30:31], -1
	s_and_b64 s[0:1], s[6:7], s[0:1]
	v_cmp_lt_f32_e32 vcc, s16, v139
	s_or_b64 vcc, vcc, s[0:1]
	s_cbranch_vccz .LBB0_3039
	v_cndmask_b32_e64 v160, 0, v139, s[0:1]
	v_max_f32_e32 v139, v139, v139
	v_max_f32_e32 v139, 0, v139
	v_cndmask_b32_e64 v160, v160, v139, s[30:31]
	v_exp_f32_e64 v139, -v160
	s_nop 0
	v_cndmask_b32_e64 v139, v139, 1.0, s[0:1]
	s_and_saveexec_b64 s[0:1], s[4:5]
	ds_write_b32 v167, v139 offset:49152
	s_or_b64 exec, exec, s[0:1]
	s_waitcnt lgkmcnt(0)
	ds_read_b128 v[202:205], v168 offset:49216
	ds_read_b128 v[206:209], v168 offset:49248
	ds_read_b128 v[210:213], v168 offset:49152
	ds_read_b128 v[214:217], v168 offset:49184
	v_mul_f32_e32 v196, v196, v139
	v_pk_add_f32 v[48:49], v[48:49], v[160:161] op_sel_hi:[1,0] neg_lo:[0,1] neg_hi:[0,1]
	v_pk_add_f32 v[32:33], v[32:33], v[160:161] op_sel_hi:[1,0] neg_lo:[0,1] neg_hi:[0,1]
	v_pk_add_f32 v[50:51], v[50:51], v[160:161] op_sel_hi:[1,0] neg_lo:[0,1] neg_hi:[0,1]
	v_pk_add_f32 v[34:35], v[34:35], v[160:161] op_sel_hi:[1,0] neg_lo:[0,1] neg_hi:[0,1]
	v_pk_add_f32 v[52:53], v[52:53], v[160:161] op_sel_hi:[1,0] neg_lo:[0,1] neg_hi:[0,1]
	v_pk_add_f32 v[36:37], v[36:37], v[160:161] op_sel_hi:[1,0] neg_lo:[0,1] neg_hi:[0,1]
	v_pk_add_f32 v[54:55], v[54:55], v[160:161] op_sel_hi:[1,0] neg_lo:[0,1] neg_hi:[0,1]
	v_pk_add_f32 v[38:39], v[38:39], v[160:161] op_sel_hi:[1,0] neg_lo:[0,1] neg_hi:[0,1]
	v_pk_add_f32 v[56:57], v[56:57], v[160:161] op_sel_hi:[1,0] neg_lo:[0,1] neg_hi:[0,1]
	v_pk_add_f32 v[40:41], v[40:41], v[160:161] op_sel_hi:[1,0] neg_lo:[0,1] neg_hi:[0,1]
	v_pk_add_f32 v[58:59], v[58:59], v[160:161] op_sel_hi:[1,0] neg_lo:[0,1] neg_hi:[0,1]
	v_pk_add_f32 v[42:43], v[42:43], v[160:161] op_sel_hi:[1,0] neg_lo:[0,1] neg_hi:[0,1]
	v_pk_add_f32 v[60:61], v[60:61], v[160:161] op_sel_hi:[1,0] neg_lo:[0,1] neg_hi:[0,1]
	v_pk_add_f32 v[44:45], v[44:45], v[160:161] op_sel_hi:[1,0] neg_lo:[0,1] neg_hi:[0,1]
	v_pk_add_f32 v[62:63], v[62:63], v[160:161] op_sel_hi:[1,0] neg_lo:[0,1] neg_hi:[0,1]
	v_pk_add_f32 v[46:47], v[46:47], v[160:161] op_sel_hi:[1,0] neg_lo:[0,1] neg_hi:[0,1]
	v_add_f32_e32 v197, v197, v160
	s_or_b64 s[30:31], s[30:31], s[6:7]
	s_waitcnt lgkmcnt(0)
	v_pk_mul_f32 v[14:15], v[14:15], v[208:209]
	v_pk_mul_f32 v[10:11], v[10:11], v[204:205]
	v_pk_mul_f32 v[6:7], v[6:7], v[216:217]
	v_pk_mul_f32 v[2:3], v[2:3], v[212:213]
	v_pk_mul_f32 v[12:13], v[12:13], v[206:207]
	v_pk_mul_f32 v[8:9], v[8:9], v[202:203]
	v_pk_mul_f32 v[4:5], v[4:5], v[214:215]
	v_pk_mul_f32 v[0:1], v[0:1], v[210:211]
	v_pk_mul_f32 v[30:31], v[30:31], v[208:209]
	v_pk_mul_f32 v[26:27], v[26:27], v[204:205]
	v_pk_mul_f32 v[22:23], v[22:23], v[216:217]
	v_pk_mul_f32 v[18:19], v[18:19], v[212:213]
	v_pk_mul_f32 v[28:29], v[28:29], v[206:207]
	v_pk_mul_f32 v[24:25], v[24:25], v[202:203]
	v_pk_mul_f32 v[20:21], v[20:21], v[214:215]
	v_pk_mul_f32 v[16:17], v[16:17], v[210:211]

.LBB0_3047:
	v_max_f32_e32 v64, v49, v49
	v_max_f32_e32 v65, v48, v48
	v_max_f32_e32 v64, v65, v64
	v_max3_f32 v65, v50, v51, v33
	v_max3_f32 v64, v64, v32, v34
	v_max3_f32 v64, v64, v35, v52
	v_max3_f32 v65, v65, v54, v55
	v_max3_f32 v64, v64, v53, v36
	v_max3_f32 v65, v65, v38, v39
	v_max3_f32 v64, v64, v37, v56
	v_max3_f32 v65, v65, v58, v59
	v_max3_f32 v64, v64, v57, v40
	v_max3_f32 v65, v65, v42, v43
	v_max3_f32 v64, v64, v41, v60
	v_max3_f32 v65, v65, v62, v63
	v_max3_f32 v64, v64, v61, v44
	v_max3_f32 v65, v65, v46, v47
	v_max3_f32 v64, v64, v45, v65
	v_mov_b32_e32 v65, v64
	s_nop 1
	v_permlane32_swap_b32_e32 v64, v65
	v_max_f32_e32 v65, v65, v65
	v_max_f32_e32 v64, v64, v64
	v_max_f32_e32 v64, v64, v65
	v_cmp_lg_f32_e32 vcc, s48, v64
	s_xor_b64 s[0:1], s[30:31], -1
	s_and_b64 s[0:1], vcc, s[0:1]
	v_cmp_lt_f32_e32 vcc, s16, v64
	s_or_b64 vcc, vcc, s[0:1]
	s_cbranch_vccz .LBB0_3051
	v_cndmask_b32_e64 v65, 0, v64, s[0:1]
	v_max_f32_e32 v64, v64, v64
	v_max_f32_e32 v64, 0, v64
	v_cndmask_b32_e64 v64, v65, v64, s[30:31]
	v_exp_f32_e64 v65, -v64
	s_nop 0
	v_cndmask_b32_e64 v65, v65, 1.0, s[0:1]
	s_and_saveexec_b64 s[0:1], s[4:5]
	ds_write_b32 v167, v65 offset:49152
	s_or_b64 exec, exec, s[0:1]
	s_waitcnt lgkmcnt(0)
	ds_read_b128 v[100:103], v168 offset:49216
	ds_read_b128 v[104:107], v168 offset:49248
	ds_read_b128 v[108:111], v168 offset:49152
	ds_read_b128 v[136:139], v168 offset:49184
	v_mul_f32_e32 v196, v196, v65
	v_pk_add_f32 v[48:49], v[48:49], v[64:65] op_sel_hi:[1,0] neg_lo:[0,1] neg_hi:[0,1]
	v_pk_add_f32 v[32:33], v[32:33], v[64:65] op_sel_hi:[1,0] neg_lo:[0,1] neg_hi:[0,1]
	v_pk_add_f32 v[50:51], v[50:51], v[64:65] op_sel_hi:[1,0] neg_lo:[0,1] neg_hi:[0,1]
	v_pk_add_f32 v[34:35], v[34:35], v[64:65] op_sel_hi:[1,0] neg_lo:[0,1] neg_hi:[0,1]
	v_pk_add_f32 v[52:53], v[52:53], v[64:65] op_sel_hi:[1,0] neg_lo:[0,1] neg_hi:[0,1]
	v_pk_add_f32 v[36:37], v[36:37], v[64:65] op_sel_hi:[1,0] neg_lo:[0,1] neg_hi:[0,1]
	v_pk_add_f32 v[54:55], v[54:55], v[64:65] op_sel_hi:[1,0] neg_lo:[0,1] neg_hi:[0,1]
	v_pk_add_f32 v[38:39], v[38:39], v[64:65] op_sel_hi:[1,0] neg_lo:[0,1] neg_hi:[0,1]
	v_pk_add_f32 v[56:57], v[56:57], v[64:65] op_sel_hi:[1,0] neg_lo:[0,1] neg_hi:[0,1]
	v_pk_add_f32 v[40:41], v[40:41], v[64:65] op_sel_hi:[1,0] neg_lo:[0,1] neg_hi:[0,1]
	v_pk_add_f32 v[58:59], v[58:59], v[64:65] op_sel_hi:[1,0] neg_lo:[0,1] neg_hi:[0,1]
	v_pk_add_f32 v[42:43], v[42:43], v[64:65] op_sel_hi:[1,0] neg_lo:[0,1] neg_hi:[0,1]
	v_pk_add_f32 v[60:61], v[60:61], v[64:65] op_sel_hi:[1,0] neg_lo:[0,1] neg_hi:[0,1]
	v_pk_add_f32 v[44:45], v[44:45], v[64:65] op_sel_hi:[1,0] neg_lo:[0,1] neg_hi:[0,1]
	v_pk_add_f32 v[62:63], v[62:63], v[64:65] op_sel_hi:[1,0] neg_lo:[0,1] neg_hi:[0,1]
	v_pk_add_f32 v[46:47], v[46:47], v[64:65] op_sel_hi:[1,0] neg_lo:[0,1] neg_hi:[0,1]
	s_waitcnt lgkmcnt(0)
	v_pk_mul_f32 v[14:15], v[14:15], v[106:107]
	v_pk_mul_f32 v[10:11], v[10:11], v[102:103]
	v_pk_mul_f32 v[6:7], v[6:7], v[138:139]
	v_pk_mul_f32 v[2:3], v[2:3], v[110:111]
	v_pk_mul_f32 v[12:13], v[12:13], v[104:105]
	v_pk_mul_f32 v[8:9], v[8:9], v[100:101]
	v_pk_mul_f32 v[4:5], v[4:5], v[136:137]
	v_pk_mul_f32 v[0:1], v[0:1], v[108:109]
	v_pk_mul_f32 v[30:31], v[30:31], v[106:107]
	v_pk_mul_f32 v[26:27], v[26:27], v[102:103]
	v_pk_mul_f32 v[22:23], v[22:23], v[138:139]
	v_pk_mul_f32 v[18:19], v[18:19], v[110:111]
	v_pk_mul_f32 v[28:29], v[28:29], v[104:105]
	v_pk_mul_f32 v[24:25], v[24:25], v[100:101]
	v_pk_mul_f32 v[20:21], v[20:21], v[136:137]
	v_pk_mul_f32 v[16:17], v[16:17], v[108:109]
